# weight-conversion loops: next tile of a 32-expert run is loaded (source + 8 MiB) before the current tile is converted/stored, decode skipped (on top of sparse L0 bias table + VALU trims + L1 dense dwo
# speedup vs baseline: 1.0113x; 1.0113x over previous
; #define LAS __attribute__((address_space(3)))
; __global__ void __launch_bounds__(NTHR, 2) fwd(Params p) {
;     extern __shared__ __attribute__((aligned(16))) unsigned char lds_raw[];
;     LAS unsigned char* lds = (LAS unsigned char*)lds_raw;
;     const int tid0 = threadIdx.x, bid = blockIdx.x, G = gridDim.x;
;     const int wv = __builtin_amdgcn_readfirstlane(tid0 >> 6);
;     const int vcu = (G % 8 == 0) ? (bid % 8) * (G / 8) + bid / 8 : bid;
;     unsigned* ctl = (unsigned*)(p.ws + WS_CTL);
;     if (tid0 < 4) ((LAS unsigned*)(lds + MISC_OFF))[tid0] = 0u;
;     __syncthreads();
;     XcdBarrier bar; bar.bar = ctl + CW_BAR; bar.x = 0; bar.st = (volatile LAS unsigned*)(lds + MISC_OFF);
;     if (N_LAUNCH_MODE == 1) bar = xcd_barrier_post(ctl + CW_BAR, (volatile LAS unsigned*)(lds + MISC_OFF));
_Z3fwd6Params:
	s_mov_b64 s[76:77], s[0:1]
	s_mov_b32 s100, 0
	s_mov_b32 s101, 0
	s_load_dword s50, s[0:1], 0xf8
	s_nop 0
	s_load_dwordx2 s[0:1], s[0:1], 0xe8
	s_mov_b32 s30, s2
	s_add_u32 s2, s76, 0xf8
	s_addc_u32 s3, s77, 0
	v_readfirstlane_b32 s8, v0
	v_writelane_b32 v252, s2, 0
	s_nop 1
	v_writelane_b32 v252, s3, 1
	s_waitcnt lgkmcnt(0)
	s_and_b32 s2, s50, 7
	s_cmp_lg_u32 s2, 0
	s_mov_b32 s2, s30
	v_writelane_b32 v252, s2, 2
	s_cbranch_scc1 .LBB0_1
	s_getpc_b64 s[98:99]

; #define LAS __attribute__((address_space(3)))
; __device__ __forceinline__ void tr_tile8(const float* __restrict__ src, int N, const float* __restrict__ ksc, float wscale, unsigned char* __restrict__ dst, int ldd, int k0, int n0, int drow0, LAS unsigned* tl, int tid) {
;     const int c4 = (tid & 15) * 4, kq = tid >> 4;
;     const float* s0 = src + (size_t)(k0 + 4 * kq) * N + n0 + c4;
;     f32x4 a = *(const f32x4*)s0, b = *(const f32x4*)(s0 + N), c = *(const f32x4*)(s0 + 2 * (size_t)N), d = *(const f32x4*)(s0 + 3 * (size_t)N);
;     float sa = wscale, sb = wscale, sc = wscale, sd = wscale;
;     if (ksc) { sa *= ksc[k0 + 4 * kq]; sb *= ksc[k0 + 4 * kq + 1]; sc *= ksc[k0 + 4 * kq + 2]; sd *= ksc[k0 + 4 * kq + 3]; }
; __device__ __forceinline__ void run_tjob(const TJob& jb, int t, LAS unsigned* tl, int tid) {
;     const int ntn = jb.N / 64, ntk = jb.K / 128, per = ntn * ntk;
;     const int bi = t / per, r = t % per, tk = r / ntn, tn = r % ntn;
;     const int n0 = tn * 64;
;     const int drow0 = jb.gu ? (256 * (n0 >> 7) + (jb.gu == 2 ? 128 : 0) + (n0 & 127)) : n0;
;     if (jb.f8) tr_tile8(jb.src + (size_t)bi * jb.sbs, jb.N, jb.ksc, W8_SCALE, (unsigned char*)jb.dst + (size_t)bi * jb.dbs, jb.ldd, tk * 128, n0, drow0, tl, tid);
;     else tr_tile(jb.src + (size_t)bi * jb.sbs, jb.N, jb.ksc, jb.dst + (size_t)bi * jb.dbs, jb.ldd, tk * 128, n0, drow0, tl, tid);
.LBB0_404:
	s_and_b64 s[48:49], s[60:61], exec
	s_cselect_b32 s33, s24, s25
	s_and_b64 s[24:25], s[58:59], exec
	s_cselect_b32 s23, s33, s23
	s_lshr_b32 s33, s36, 6
	s_lshr_b32 s24, s28, 7
	s_mul_i32 s24, s33, s24
	v_cvt_f32_u32_e32 v0, s24
	s_sub_i32 s49, 0, s24
	s_sub_i32 s25, s15, s23
	s_abs_i32 s48, s25
	v_rcp_iflag_f32_e32 v0, v0
	s_ashr_i32 s23, s25, 31
	s_load_dwordx2 s[40:41], s[40:41], 0x0
	v_mul_f32_e32 v0, 0x4f7ffffe, v0
	v_cvt_u32_f32_e32 v0, v0
	s_nop 0
	v_readfirstlane_b32 s58, v0
	s_mul_i32 s49, s49, s58
	s_mul_hi_u32 s49, s58, s49
	s_add_i32 s58, s58, s49
	s_mul_hi_u32 s49, s48, s58
	s_mul_i32 s58, s49, s24
	s_sub_i32 s48, s48, s58
	s_add_i32 s59, s49, 1
	s_sub_i32 s58, s48, s24
	s_cmp_ge_u32 s48, s24
	s_cselect_b32 s49, s59, s49
	s_cselect_b32 s48, s58, s48
	s_add_i32 s58, s49, 1
	s_cmp_ge_u32 s48, s24
	s_cselect_b32 s48, s58, s49
	s_xor_b32 s48, s48, s23
	s_sub_i32 s23, s48, s23
	v_cvt_f32_i32_e32 v0, s33
	s_mul_i32 s24, s23, s24
	s_sub_i32 s48, s25, s24
	s_sext_i32_i16 s24, s48
	v_cvt_f32_i32_e32 v1, s24
	v_rcp_iflag_f32_e32 v2, v0
	s_ashr_i32 s24, s24, 30
	s_or_b32 s49, s24, 1
	v_mul_f32_e32 v2, v1, v2
	v_trunc_f32_e32 v2, v2
	v_fma_f32 v1, -v2, v0, v1
	v_cvt_i32_f32_e32 v2, v2
	v_cmp_ge_f32_e64 s[24:25], |v1|, v0
	s_and_b64 s[24:25], s[24:25], exec
	s_cselect_b32 s24, s49, 0
	v_readfirstlane_b32 s25, v2
	s_add_i32 s24, s25, s24
	s_sext_i32_i16 s59, s24
	s_mul_i32 s24, s24, s33
	s_sub_i32 s24, s48, s24
	s_sext_i32_i16 s25, s24
	s_ashr_i32 s24, s23, 31
	s_mul_i32 s33, s86, s24
	s_mul_hi_u32 s48, s86, s23
	s_add_i32 s33, s48, s33
	s_mul_i32 s48, s87, s23
	s_add_i32 s49, s33, s48
	s_mul_i32 s48, s86, s23
	s_lshl_b32 s58, s25, 6
	s_lshl_b64 s[48:49], s[48:49], 2
	s_waitcnt lgkmcnt(0)
	s_add_u32 s48, s40, s48
	s_addc_u32 s49, s41, s49
	s_lshl_b32 s40, s59, 7
	v_add_u32_e32 v20, s40, v17
	v_mad_u64_u32 v[0:1], s[60:61], v20, s36, 0
	v_ashrrev_i32_e32 v21, 31, v20
	v_mov_b32_e32 v2, v1
	v_mad_u64_u32 v[2:3], s[60:61], v21, s36, v[2:3]
	v_mov_b32_e32 v1, v2
	v_lshl_add_u64 v[0:1], v[0:1], 2, s[48:49]
	s_ashr_i32 s59, s58, 31
	v_lshl_add_u64 v[0:1], s[58:59], 2, v[0:1]
	v_lshl_add_u64 v[0:1], v[0:1], 0, v[232:233]
	s_or_b32 s100, s86, s87
	s_cmp_lg_u32 s100, 0
	s_cselect_b32 s100, s25, -1
	v_mov_b64_e32 v[64:65], v[0:1]
	s_lshl_b64 s[48:49], s[36:37], 2
	v_lshl_add_u64 v[2:3], v[0:1], 0, s[48:49]
	global_load_dwordx4 v[8:11], v[0:1], off
	global_load_dwordx4 v[12:15], v[2:3], off
	v_lshl_add_u64 v[0:1], v[2:3], 0, s[48:49]
	v_lshl_add_u64 v[4:5], v[0:1], 0, s[48:49]
	global_load_dwordx4 v[0:3], v[0:1], off
	s_nop 0
	global_load_dwordx4 v[4:7], v[4:5], off
	s_cmp_eq_u64 s[8:9], 0
	s_cbranch_scc1 .LBB0_443
	v_lshl_add_u64 v[20:21], v[20:21], 2, s[8:9]
	global_load_dwordx4 v[28:31], v[20:21], off
	s_waitcnt vmcnt(0)
	v_pk_mul_f32 v[22:23], v[28:29], s[16:17] op_sel_hi:[1,0]
	v_pk_mul_f32 v[20:21], v[30:31], s[16:17] op_sel_hi:[1,0]

; #define LAS __attribute__((address_space(3)))
; __device__ __forceinline__ void tr_tile8(const float* __restrict__ src, int N, const float* __restrict__ ksc, float wscale, unsigned char* __restrict__ dst, int ldd, int k0, int n0, int drow0, LAS unsigned* tl, int tid) {
;     const int c4 = (tid & 15) * 4, kq = tid >> 4;
;     const float* s0 = src + (size_t)(k0 + 4 * kq) * N + n0 + c4;
;     f32x4 a = *(const f32x4*)s0, b = *(const f32x4*)(s0 + N), c = *(const f32x4*)(s0 + 2 * (size_t)N), d = *(const f32x4*)(s0 + 3 * (size_t)N);
;     float sa = wscale, sb = wscale, sc = wscale, sd = wscale;
;     if (ksc) { sa *= ksc[k0 + 4 * kq]; sb *= ksc[k0 + 4 * kq + 1]; sc *= ksc[k0 + 4 * kq + 2]; sd *= ksc[k0 + 4 * kq + 3]; }
; #pragma unroll
;     for (int j = 0; j < 4; ++j) tl[(c4 + j) * 33 + kq] = pk4_fp8(a[j] * sa, b[j] * sb, c[j] * sc, d[j] * sd);
;     __syncthreads();
;     const int n = tid >> 3, seg = tid & 7;
;     unsigned w[4];
; #pragma unroll
;     for (int q = 0; q < 4; ++q) w[q] = tl[n * 33 + seg * 4 + q];
;     *(u32x4*)(dst + (size_t)(drow0 + n) * ldd + k0 + seg * 16) = (u32x4){w[0], w[1], w[2], w[3]};
;     __syncthreads();
.Lcv1_proc:
	s_mov_b32 s101, 0
	s_cmp_lt_i32 s100, 0
	s_cbranch_scc1 .Lcv1_nx
	s_cmp_lt_i32 s23, 30
	s_cbranch_scc0 .Lcv1_nx
	s_cmp_eq_u32 s50, 0x100
	s_cbranch_scc0 .Lcv1_nx
	s_mov_b64 vcc, 0x800000
	v_lshl_add_u64 v[64:65], v[64:65], 0, vcc
	s_lshl_b64 s[48:49], s[36:37], 2
	v_lshl_add_u64 v[72:73], v[64:65], 0, s[48:49]
	global_load_dwordx4 v[80:83], v[64:65], off
	global_load_dwordx4 v[84:87], v[72:73], off
	v_lshl_add_u64 v[72:73], v[72:73], 0, s[48:49]
	v_lshl_add_u64 v[74:75], v[72:73], 0, s[48:49]
	global_load_dwordx4 v[88:91], v[72:73], off
	global_load_dwordx4 v[92:95], v[74:75], off
	s_mov_b32 s101, 1
.Lcv1_nx:
	v_mul_f32_e32 v8, v8, v22
	v_mul_f32_e32 v12, v12, v23
	v_cvt_pk_fp8_f32 v8, v8, v12
	v_mul_f32_e32 v9, v9, v22
	v_mul_f32_e32 v12, v13, v23
	v_cvt_pk_fp8_f32 v9, v9, v12
	s_lshl_b32 s8, s25, 7
	s_and_b32 s8, s8, 0xffffff00
	v_mul_f32_e32 v0, v0, v20
	v_mul_f32_e32 v4, v4, v21
	s_and_b32 s9, s58, 64
	s_or_b32 s8, s8, s29
	v_cvt_pk_fp8_f32 v8, v0, v4 op_sel:[0,0,1]
	v_mul_f32_e32 v0, v1, v20
	v_mul_f32_e32 v1, v5, v21
	s_or_b32 s25, s8, s9
	v_cvt_pk_fp8_f32 v9, v0, v1 op_sel:[0,0,1]
	v_mul_f32_e32 v0, v10, v22
	v_mul_f32_e32 v1, v14, v23
	s_and_b64 s[8:9], s[56:57], exec
	v_cvt_pk_fp8_f32 v0, v0, v1
	v_mul_f32_e32 v1, v11, v22
	v_mul_f32_e32 v5, v15, v23
	s_mul_i32 s8, s62, s24
	s_mul_hi_u32 s9, s62, s23
	v_cvt_pk_fp8_f32 v1, v1, v5
	s_cselect_b32 s25, s58, s25
	s_add_i32 s8, s9, s8
	s_mul_i32 s9, s63, s23
	s_add_i32 s9, s8, s9
	s_mul_i32 s8, s62, s23
	v_mul_f32_e32 v2, v2, v20
	v_mul_f32_e32 v4, v6, v21
	v_cvt_pk_fp8_f32 v0, v2, v4 op_sel:[0,0,1]
	v_mul_f32_e32 v2, v3, v20
	v_mul_f32_e32 v3, v7, v21
	s_add_u32 s8, s42, s8
	v_cvt_pk_fp8_f32 v1, v2, v3 op_sel:[0,0,1]
	s_addc_u32 s9, s43, s9
	v_add_u32_e32 v6, s25, v24
	v_mov_b64_e32 v[4:5], s[8:9]
	v_mad_u64_u32 v[4:5], s[8:9], v6, s28, v[4:5]
	ds_write2_b32 v25, v8, v9 offset1:33
	ds_write2_b32 v25, v0, v1 offset0:66 offset1:99
	s_waitcnt lgkmcnt(0)
	s_barrier
	ds_read2_b32 v[0:1], v26 offset1:1
	ds_read2_b32 v[2:3], v26 offset0:2 offset1:3
	v_ashrrev_i32_e32 v7, 31, v6
	v_mov_b32_e32 v6, v5
	v_mad_u64_u32 v[6:7], s[8:9], v7, s28, v[6:7]
	v_mov_b32_e32 v5, v6
	s_ashr_i32 s41, s40, 31
	v_lshl_add_u64 v[4:5], v[4:5], 0, s[40:41]
	s_add_i32 s15, s15, s50
	v_readlane_b32 s49, v255, 49
	s_mov_b64 s[86:87], 0x5000
	v_lshl_add_u64 v[4:5], v[4:5], 0, v[18:19]
	s_cmpk_gt_i32 s15, 0x6cef
	s_waitcnt lgkmcnt(0)
	global_store_dwordx4 v[4:5], v[0:3], off
	s_barrier
	s_cbranch_scc1 .LBB0_447
	s_cmp_eq_u32 s101, 1
	s_cbranch_scc0 .LBB0_407
	s_add_i32 s23, s23, 2
	s_mov_b32 s25, s100
	s_waitcnt vmcnt(1)
	v_mov_b64_e32 v[8:9], v[80:81]
	v_mov_b64_e32 v[10:11], v[82:83]
	v_mov_b64_e32 v[12:13], v[84:85]
	v_mov_b64_e32 v[14:15], v[86:87]
	v_mov_b64_e32 v[0:1], v[88:89]
	v_mov_b64_e32 v[2:3], v[90:91]
	v_mov_b64_e32 v[4:5], v[92:93]
	v_mov_b64_e32 v[6:7], v[94:95]
	s_branch .Lcv1_proc

; #define LAS __attribute__((address_space(3)))
; __device__ __forceinline__ void tr_tile8(const float* __restrict__ src, int N, const float* __restrict__ ksc, float wscale, unsigned char* __restrict__ dst, int ldd, int k0, int n0, int drow0, LAS unsigned* tl, int tid) {
;     const int c4 = (tid & 15) * 4, kq = tid >> 4;
;     const float* s0 = src + (size_t)(k0 + 4 * kq) * N + n0 + c4;
;     f32x4 a = *(const f32x4*)s0, b = *(const f32x4*)(s0 + N), c = *(const f32x4*)(s0 + 2 * (size_t)N), d = *(const f32x4*)(s0 + 3 * (size_t)N);
;     float sa = wscale, sb = wscale, sc = wscale, sd = wscale;
;     if (ksc) { sa *= ksc[k0 + 4 * kq]; sb *= ksc[k0 + 4 * kq + 1]; sc *= ksc[k0 + 4 * kq + 2]; sd *= ksc[k0 + 4 * kq + 3]; }
; __device__ __forceinline__ void run_tjob(const TJob& jb, int t, LAS unsigned* tl, int tid) {
;     const int ntn = jb.N / 64, ntk = jb.K / 128, per = ntn * ntk;
;     const int bi = t / per, r = t % per, tk = r / ntn, tn = r % ntn;
;     const int n0 = tn * 64;
;     const int drow0 = jb.gu ? (256 * (n0 >> 7) + (jb.gu == 2 ? 128 : 0) + (n0 & 127)) : n0;
;     if (jb.f8) tr_tile8(jb.src + (size_t)bi * jb.sbs, jb.N, jb.ksc, W8_SCALE, (unsigned char*)jb.dst + (size_t)bi * jb.dbs, jb.ldd, tk * 128, n0, drow0, tl, tid);
;     else tr_tile(jb.src + (size_t)bi * jb.sbs, jb.N, jb.ksc, jb.dst + (size_t)bi * jb.dbs, jb.ldd, tk * 128, n0, drow0, tl, tid);
.LBB0_586:
	s_and_b64 s[48:49], s[60:61], exec
	s_cselect_b32 s33, s24, s25
	s_and_b64 s[24:25], s[58:59], exec
	s_cselect_b32 s23, s33, s23
	s_lshr_b32 s33, s36, 6
	s_lshr_b32 s24, s28, 7
	s_mul_i32 s24, s33, s24
	v_cvt_f32_u32_e32 v0, s24
	s_sub_i32 s49, 0, s24
	s_sub_i32 s25, s15, s23
	s_abs_i32 s48, s25
	v_rcp_iflag_f32_e32 v0, v0
	s_ashr_i32 s23, s25, 31
	v_mul_f32_e32 v0, 0x4f7ffffe, v0
	v_cvt_u32_f32_e32 v0, v0
	s_nop 0
	v_readfirstlane_b32 s58, v0
	s_mul_i32 s49, s49, s58
	s_mul_hi_u32 s49, s58, s49
	s_add_i32 s58, s58, s49
	s_mul_hi_u32 s49, s48, s58
	s_mul_i32 s58, s49, s24
	s_sub_i32 s48, s48, s58
	s_add_i32 s59, s49, 1
	s_sub_i32 s58, s48, s24
	s_cmp_ge_u32 s48, s24
	s_cselect_b32 s49, s59, s49
	s_cselect_b32 s48, s58, s48
	s_add_i32 s58, s49, 1
	s_cmp_ge_u32 s48, s24
	s_cselect_b32 s48, s58, s49
	s_xor_b32 s48, s48, s23
	s_sub_i32 s23, s48, s23
	v_cvt_f32_i32_e32 v0, s33
	s_mul_i32 s24, s23, s24
	s_sub_i32 s58, s25, s24
	s_sext_i32_i16 s24, s58
	v_cvt_f32_i32_e32 v1, s24
	v_rcp_iflag_f32_e32 v2, v0
	s_ashr_i32 s24, s24, 30
	s_or_b32 s59, s24, 1
	s_load_dwordx2 s[48:49], s[64:65], 0x0
	v_mul_f32_e32 v2, v1, v2
	v_trunc_f32_e32 v2, v2
	v_fma_f32 v1, -v2, v0, v1
	v_cvt_i32_f32_e32 v2, v2
	v_cmp_ge_f32_e64 s[24:25], |v1|, v0
	s_and_b64 s[24:25], s[24:25], exec
	s_cselect_b32 s24, s59, 0
	v_readfirstlane_b32 s25, v2
	s_add_i32 s24, s25, s24
	s_sext_i32_i16 s61, s24
	s_mul_i32 s24, s24, s33
	s_sub_i32 s24, s58, s24
	s_sext_i32_i16 s25, s24
	s_ashr_i32 s24, s23, 31
	s_mul_i32 s33, s66, s24
	s_mul_hi_u32 s58, s66, s23
	s_add_i32 s33, s58, s33
	s_mul_i32 s58, s67, s23
	s_add_i32 s59, s33, s58
	s_mul_i32 s58, s66, s23
	s_lshl_b32 s60, s25, 6
	s_lshl_b64 s[58:59], s[58:59], 2
	s_waitcnt lgkmcnt(0)
	s_add_u32 s48, s48, s58
	s_addc_u32 s49, s49, s59
	s_lshl_b32 s58, s61, 7
	v_add_u32_e32 v20, s58, v17
	v_mad_u64_u32 v[0:1], s[64:65], v20, s36, 0
	v_ashrrev_i32_e32 v21, 31, v20
	v_mov_b32_e32 v2, v1
	v_mad_u64_u32 v[2:3], s[64:65], v21, s36, v[2:3]
	v_mov_b32_e32 v1, v2
	v_lshl_add_u64 v[0:1], v[0:1], 2, s[48:49]
	s_ashr_i32 s61, s60, 31
	v_lshl_add_u64 v[0:1], s[60:61], 2, v[0:1]
	v_lshl_add_u64 v[0:1], v[0:1], 0, v[232:233]
	s_or_b32 s100, s66, s67
	s_cmp_lg_u32 s100, 0
	s_cselect_b32 s100, s25, -1
	v_mov_b64_e32 v[64:65], v[0:1]
	s_lshl_b64 s[48:49], s[36:37], 2
	v_lshl_add_u64 v[2:3], v[0:1], 0, s[48:49]
	global_load_dwordx4 v[8:11], v[0:1], off
	global_load_dwordx4 v[12:15], v[2:3], off
	v_lshl_add_u64 v[0:1], v[2:3], 0, s[48:49]
	v_lshl_add_u64 v[4:5], v[0:1], 0, s[48:49]
	global_load_dwordx4 v[0:3], v[0:1], off
	s_nop 0
	global_load_dwordx4 v[4:7], v[4:5], off
	s_cmp_eq_u64 s[8:9], 0
	s_cbranch_scc1 .LBB0_625
	v_lshl_add_u64 v[20:21], v[20:21], 2, s[8:9]
	global_load_dwordx4 v[28:31], v[20:21], off
	s_waitcnt vmcnt(0)
	v_pk_mul_f32 v[22:23], v[28:29], s[16:17] op_sel_hi:[1,0]
	v_pk_mul_f32 v[20:21], v[30:31], s[16:17] op_sel_hi:[1,0]

; #define LAS __attribute__((address_space(3)))
; __device__ __forceinline__ void tr_tile8(const float* __restrict__ src, int N, const float* __restrict__ ksc, float wscale, unsigned char* __restrict__ dst, int ldd, int k0, int n0, int drow0, LAS unsigned* tl, int tid) {
;     const int c4 = (tid & 15) * 4, kq = tid >> 4;
;     const float* s0 = src + (size_t)(k0 + 4 * kq) * N + n0 + c4;
;     f32x4 a = *(const f32x4*)s0, b = *(const f32x4*)(s0 + N), c = *(const f32x4*)(s0 + 2 * (size_t)N), d = *(const f32x4*)(s0 + 3 * (size_t)N);
;     float sa = wscale, sb = wscale, sc = wscale, sd = wscale;
;     if (ksc) { sa *= ksc[k0 + 4 * kq]; sb *= ksc[k0 + 4 * kq + 1]; sc *= ksc[k0 + 4 * kq + 2]; sd *= ksc[k0 + 4 * kq + 3]; }
; #pragma unroll
;     for (int j = 0; j < 4; ++j) tl[(c4 + j) * 33 + kq] = pk4_fp8(a[j] * sa, b[j] * sb, c[j] * sc, d[j] * sd);
;     __syncthreads();
;     const int n = tid >> 3, seg = tid & 7;
;     unsigned w[4];
; #pragma unroll
;     for (int q = 0; q < 4; ++q) w[q] = tl[n * 33 + seg * 4 + q];
;     *(u32x4*)(dst + (size_t)(drow0 + n) * ldd + k0 + seg * 16) = (u32x4){w[0], w[1], w[2], w[3]};
;     __syncthreads();
.Lcv2_nx:
	v_mul_f32_e32 v8, v8, v22
	v_mul_f32_e32 v12, v12, v23
	v_cvt_pk_fp8_f32 v8, v8, v12
	v_mul_f32_e32 v9, v9, v22
	v_mul_f32_e32 v12, v13, v23
	v_cvt_pk_fp8_f32 v9, v9, v12
	s_lshl_b32 s8, s25, 7
	s_and_b32 s8, s8, 0xffffff00
	v_mul_f32_e32 v0, v0, v20
	v_mul_f32_e32 v4, v4, v21
	s_and_b32 s9, s60, 64
	s_or_b32 s8, s8, s29
	v_cvt_pk_fp8_f32 v8, v0, v4 op_sel:[0,0,1]
	v_mul_f32_e32 v0, v1, v20
	v_mul_f32_e32 v1, v5, v21
	s_or_b32 s25, s8, s9
	v_cvt_pk_fp8_f32 v9, v0, v1 op_sel:[0,0,1]
	v_mul_f32_e32 v0, v10, v22
	v_mul_f32_e32 v1, v14, v23
	s_and_b64 s[8:9], s[56:57], exec
	v_cvt_pk_fp8_f32 v0, v0, v1
	v_mul_f32_e32 v1, v11, v22
	v_mul_f32_e32 v5, v15, v23
	s_mul_i32 s8, s62, s24
	s_mul_hi_u32 s9, s62, s23
	v_cvt_pk_fp8_f32 v1, v1, v5
	s_cselect_b32 s25, s60, s25
	s_add_i32 s8, s9, s8
	s_mul_i32 s9, s63, s23
	s_add_i32 s9, s8, s9
	s_mul_i32 s8, s62, s23
	v_mul_f32_e32 v2, v2, v20
	v_mul_f32_e32 v4, v6, v21
	v_cvt_pk_fp8_f32 v0, v2, v4 op_sel:[0,0,1]
	v_mul_f32_e32 v2, v3, v20
	v_mul_f32_e32 v3, v7, v21
	s_add_u32 s8, s54, s8
	v_cvt_pk_fp8_f32 v1, v2, v3 op_sel:[0,0,1]
	s_addc_u32 s9, s55, s9
	v_add_u32_e32 v6, s25, v24
	v_mov_b64_e32 v[4:5], s[8:9]
	v_mad_u64_u32 v[4:5], s[8:9], v6, s28, v[4:5]
	ds_write2_b32 v25, v8, v9 offset1:33
	ds_write2_b32 v25, v0, v1 offset0:66 offset1:99
	s_waitcnt lgkmcnt(0)
	s_barrier
	ds_read2_b32 v[0:1], v26 offset1:1
	ds_read2_b32 v[2:3], v26 offset0:2 offset1:3
	v_ashrrev_i32_e32 v7, 31, v6
	v_mov_b32_e32 v6, v5
	v_mad_u64_u32 v[6:7], s[8:9], v7, s28, v[6:7]
	v_mov_b32_e32 v5, v6
	s_ashr_i32 s59, s58, 31
	v_lshl_add_u64 v[4:5], v[4:5], 0, s[58:59]
	s_add_i32 s15, s15, s50
	v_readlane_b32 s49, v255, 49
	s_mov_b64 s[86:87], 0x5000
	v_lshl_add_u64 v[4:5], v[4:5], 0, v[18:19]
	s_cmpk_gt_i32 s15, 0x6cef
	s_waitcnt lgkmcnt(0)
	global_store_dwordx4 v[4:5], v[0:3], off
	s_barrier
	s_cbranch_scc1 .LBB0_629
	s_cmp_eq_u32 s101, 1
	s_cbranch_scc0 .LBB0_589
	s_add_i32 s23, s23, 2
	s_mov_b32 s25, s100
	s_waitcnt vmcnt(1)
	v_mov_b64_e32 v[8:9], v[80:81]
	v_mov_b64_e32 v[10:11], v[82:83]
	v_mov_b64_e32 v[12:13], v[84:85]
	v_mov_b64_e32 v[14:15], v[86:87]
	v_mov_b64_e32 v[0:1], v[88:89]
	v_mov_b64_e32 v[2:3], v[90:91]
	v_mov_b64_e32 v[4:5], v[92:93]
	v_mov_b64_e32 v[6:7], v[94:95]
	s_branch .Lcv2_proc
